# same as the previous best; the two v_readlane -> v_mov SGPR hand-offs in the in-projection side-stream set-up padded to two wait states
# baseline (speedup 1.0000x reference)
.LBB0_236:
	v_and_b32_e32 v2, 15, v0
	v_or_b32_e32 v3, s63, v2
	v_lshlrev_b32_e32 v6, 4, v0
	v_lshlrev_b32_e32 v4, 6, v3
	v_and_b32_e32 v5, 48, v0
	s_movk_i32 s0, 0x3c0
	v_and_b32_e32 v6, 0xfffffc00, v6
	v_lshlrev_b32_e32 v3, 2, v3
	v_and_or_b32 v4, v4, s0, v5
	v_add_u32_e32 v7, s65, v6
	v_and_b32_e32 v3, 32, v3
	v_lshlrev_b32_e32 v0, 2, v0
	v_bitop3_b32 v4, v4, v7, v3 bitop3:0xde
	v_lshl_or_b32 v2, v2, 6, v5
	v_add_u32_e32 v3, s67, v6
	v_and_b32_e32 v0, 32, v0
	v_bitop3_b32 v177, v2, v3, v0 bitop3:0xde
	v_mbcnt_lo_u32_b32 v0, -1, 0
	v_mbcnt_hi_u32_b32 v0, -1, v0
	v_and_b32_e32 v5, 15, v0
	v_lshrrev_b32_e32 v0, 4, v0
	v_bfe_u32 v6, v5, 1, 3
	v_and_b32_e32 v7, 1, v6
	v_lshlrev_b32_e32 v7, 1, v7
	v_and_or_b32 v6, v6, 4, v7
	v_xor_b32_e32 v0, v0, v6
	v_lshlrev_b32_e32 v0, 4, v0
	v_lshl_add_u32 v0, v5, 7, v0
	v_add_u32_e32 v4, s65, v0
	v_xor_b32_e32 v212, 64, v4
	v_add_u32_e32 v177, s67, v0
	v_xor_b32_e32 v213, 64, v177
	v_add_u32_e32 v213, 0x10000, v213
	s_waitcnt vmcnt(2)
	s_barrier
	s_add_i32 m0, s97, 0x18000
	v_lshl_add_u64 v[2:3], s[6:7], 0, v[160:161]
	v_lshl_add_u64 v[2:3], v[2:3], 0, s[52:53]
	global_load_lds_dwordx4 v[2:3], off
	v_mov_b32_e32 v163, v161
	s_add_i32 m0, s97, 0x1a000
	s_add_u32 s0, s70, 0x32000080
	v_lshl_add_u64 v[2:3], s[6:7], 0, v[162:163]
	v_lshl_add_u64 v[2:3], v[2:3], 0, s[52:53]
	s_addc_u32 s1, s71, 0
	s_add_i32 s31, s97, 0x8000
	global_load_lds_dwordx4 v[2:3], off
	s_mov_b32 m0, s31
	s_add_i32 s42, s97, 0xa000
	v_mov_b32_e32 v0, 0
	global_load_lds_dwordx4 v164, s[0:1]
	s_mov_b32 m0, s42
	s_mov_b32 s47, 0
	global_load_lds_dwordx4 v166, s[0:1]
	s_add_u32 s0, s6, 0x8080
	s_addc_u32 s1, s7, 0
	s_add_i32 m0, s97, 0x1c000
	v_add_u32_e32 v178, 0, v4
	global_load_lds_dwordx4 v160, s[0:1]
	s_add_i32 m0, s97, 0x1e000
	v_mov_b32_e32 v168, v160
	global_load_lds_dwordx4 v162, s[0:1]
	s_waitcnt vmcnt(6)
	v_mov_b32_e32 v160, v1
	s_mov_b32 s43, s82
	s_mov_b32 s83, s44
	v_mov_b32_e32 v1, v0
	v_mov_b32_e32 v2, v0
	v_mov_b32_e32 v3, v0
	v_mov_b32_e32 v4, v0
	v_mov_b32_e32 v5, v0
	v_mov_b32_e32 v6, v0
	v_mov_b32_e32 v7, v0
	v_mov_b32_e32 v8, v0
	v_mov_b32_e32 v9, v0
	v_mov_b32_e32 v10, v0
	v_mov_b32_e32 v11, v0
	v_mov_b32_e32 v12, v0
	v_mov_b32_e32 v13, v0
	v_mov_b32_e32 v14, v0
	v_mov_b32_e32 v15, v0
	v_mov_b32_e32 v16, v0
	v_mov_b32_e32 v17, v0
	v_mov_b32_e32 v18, v0
	v_mov_b32_e32 v19, v0
	v_mov_b32_e32 v20, v0
	v_mov_b32_e32 v21, v0
	v_mov_b32_e32 v22, v0
	v_mov_b32_e32 v23, v0
	v_mov_b32_e32 v24, v0
	v_mov_b32_e32 v25, v0
	v_mov_b32_e32 v26, v0
	v_mov_b32_e32 v27, v0
	v_mov_b32_e32 v28, v0
	v_mov_b32_e32 v29, v0
	v_mov_b32_e32 v30, v0
	v_mov_b32_e32 v31, v0
	v_mov_b32_e32 v36, v0
	v_mov_b32_e32 v37, v0
	v_mov_b32_e32 v38, v0
	v_mov_b32_e32 v39, v0
	v_mov_b32_e32 v44, v0
	v_mov_b32_e32 v45, v0
	v_mov_b32_e32 v46, v0
	v_mov_b32_e32 v47, v0
	v_mov_b32_e32 v32, v0
	v_mov_b32_e32 v33, v0
	v_mov_b32_e32 v34, v0
	v_mov_b32_e32 v35, v0
	v_mov_b32_e32 v40, v0
	v_mov_b32_e32 v41, v0
	v_mov_b32_e32 v42, v0
	v_mov_b32_e32 v43, v0
	v_mov_b32_e32 v48, v0
	v_mov_b32_e32 v49, v0
	v_mov_b32_e32 v50, v0
	v_mov_b32_e32 v51, v0
	v_mov_b32_e32 v52, v0
	v_mov_b32_e32 v53, v0
	v_mov_b32_e32 v54, v0
	v_mov_b32_e32 v55, v0
	v_mov_b32_e32 v56, v0
	v_mov_b32_e32 v57, v0
	v_mov_b32_e32 v58, v0
	v_mov_b32_e32 v59, v0
	v_mov_b32_e32 v60, v0
	v_mov_b32_e32 v61, v0
	v_mov_b32_e32 v62, v0
	v_mov_b32_e32 v63, v0
	v_mov_b32_e32 v64, v0
	v_mov_b32_e32 v65, v0
	v_mov_b32_e32 v66, v0
	v_mov_b32_e32 v67, v0
	v_mov_b32_e32 v68, v0
	v_mov_b32_e32 v69, v0
	v_mov_b32_e32 v70, v0
	v_mov_b32_e32 v71, v0
	v_mov_b32_e32 v72, v0
	v_mov_b32_e32 v73, v0
	v_mov_b32_e32 v74, v0
	v_mov_b32_e32 v75, v0
	v_mov_b32_e32 v76, v0
	v_mov_b32_e32 v77, v0
	v_mov_b32_e32 v78, v0
	v_mov_b32_e32 v79, v0
	v_mov_b32_e32 v80, v0
	v_mov_b32_e32 v81, v0
	v_mov_b32_e32 v82, v0
	v_mov_b32_e32 v83, v0
	v_mov_b32_e32 v84, v0
	v_mov_b32_e32 v85, v0
	v_mov_b32_e32 v86, v0
	v_mov_b32_e32 v87, v0
	v_mov_b32_e32 v88, v0
	v_mov_b32_e32 v89, v0
	v_mov_b32_e32 v90, v0
	v_mov_b32_e32 v91, v0
	v_mov_b32_e32 v92, v0
	v_mov_b32_e32 v93, v0
	v_mov_b32_e32 v94, v0
	v_mov_b32_e32 v95, v0
	v_mov_b32_e32 v96, v0
	v_mov_b32_e32 v97, v0
	v_mov_b32_e32 v98, v0
	v_mov_b32_e32 v99, v0
	v_mov_b32_e32 v100, v0
	v_mov_b32_e32 v101, v0
	v_mov_b32_e32 v102, v0
	v_mov_b32_e32 v103, v0
	v_mov_b32_e32 v104, v0
	v_mov_b32_e32 v105, v0
	v_mov_b32_e32 v106, v0
	v_mov_b32_e32 v107, v0
	v_mov_b32_e32 v108, v0
	v_mov_b32_e32 v109, v0
	v_mov_b32_e32 v110, v0
	v_mov_b32_e32 v111, v0
	v_mov_b32_e32 v112, v0
	v_mov_b32_e32 v113, v0
	v_mov_b32_e32 v114, v0
	v_mov_b32_e32 v115, v0
	v_mov_b32_e32 v116, v0
	v_mov_b32_e32 v117, v0
	v_mov_b32_e32 v118, v0
	v_mov_b32_e32 v119, v0
	v_mov_b32_e32 v120, v0
	v_mov_b32_e32 v121, v0
	v_mov_b32_e32 v122, v0
	v_mov_b32_e32 v123, v0
	v_mov_b32_e32 v124, v0
	v_mov_b32_e32 v125, v0
	v_mov_b32_e32 v126, v0
	v_mov_b32_e32 v127, v0
	v_mbcnt_lo_u32_b32 v244, -1, 0
	v_mbcnt_hi_u32_b32 v244, -1, v244
	v_lshrrev_b32_e32 v245, 3, v244
	v_and_b32_e32 v246, 7, v244
	v_lshlrev_b32_e32 v248, 17, v245
	v_lshl_or_b32 v248, v246, 4, v248
	v_lshrrev_b32_e32 v247, 1, v246
	v_and_b32_e32 v246, 1, v246
	v_lshlrev_b32_e32 v249, 15, v247
	v_lshl_or_b32 v249, v246, 13, v249
	v_lshl_or_b32 v249, v245, 3, v249
	v_mov_b32_e32 v252, 0x43800000
	v_mov_b32_e32 v253, 0x43800000
	v_readlane_b32 s32, v255, 54
	s_nop 1
	v_mov_b32_e32 v250, s32
	v_readlane_b32 s32, v255, 55
	s_nop 1
	v_mov_b32_e32 v251, s32
	s_barrier
